# combined version with the store-draining vmcnt(0) removed at the mixer work-queue publish barrier (atomic result is already retired by each unit's mid-unit vmcnt(0))
# baseline (speedup 1.0000x reference)
.LBB0_814:
	s_waitcnt lgkmcnt(0)
	s_barrier
	s_and_saveexec_b64 s[6:7], s[4:5]
	s_cbranch_execz .LBB0_453
	v_add_u32_e32 v2, s3, v243
	v_cmp_eq_u32_e32 vcc, -1, v176
	s_nop 1
	v_cndmask_b32_e32 v176, v176, v2, vcc
	v_mov_b32_e32 v2, s70
	ds_write_b32 v2, v176
	v_mov_b32_e32 v2, s48
	ds_write_b32 v2, v177
	s_branch .LBB0_453

.LBB0_1973:
	s_waitcnt lgkmcnt(0)
	s_barrier
	s_and_saveexec_b64 s[6:7], s[4:5]
	s_cbranch_execz .LBB0_1706
	v_add_u32_e32 v2, s3, v243
	v_cmp_eq_u32_e32 vcc, -1, v170
	s_nop 1
	v_cndmask_b32_e32 v170, v170, v2, vcc
	v_mov_b32_e32 v2, s85
	ds_write_b32 v2, v170
	v_mov_b32_e32 v2, s86
	ds_write_b32 v2, v171
	s_branch .LBB0_1706
